# P14 K-loop: stage DMAs issued at the head of each load half (earlier by one fragment-read burst)
# speedup vs baseline: 1.0012x; 1.0012x over previous
.LBB0_1458:
	s_ashr_i32 s41, s40, 31
	s_lshl_b64 s[4:5], s[40:41], 21
	s_add_u32 s42, s6, s4
	s_addc_u32 s43, s7, s5
	s_and_b64 s[4:5], s[38:39], exec
	s_cselect_b32 s41, s43, s49
	s_cselect_b32 s68, s42, s48
	s_ashr_i32 s37, s36, 31
	s_lshl_b64 s[4:5], s[36:37], 21
	s_add_u32 s44, s8, s4
	s_addc_u32 s45, s9, s5
	s_and_b64 s[4:5], s[38:39], exec
	s_cselect_b32 s37, s45, s51
	s_cselect_b32 s69, s44, s50
	s_add_u32 s70, s68, 0x80
	s_addc_u32 s71, s41, 0
	s_add_u32 s72, s50, 0x100
	s_addc_u32 s73, s51, 0
	s_add_u32 s4, s48, 0x100080
	s_addc_u32 s5, s49, 0
	v_lshl_add_u64 v[112:113], s[4:5], 0, v[210:211]
	v_lshl_add_u64 v[114:115], s[4:5], 0, v[212:213]
	s_mov_b32 s74, -2
	s_mov_b64 s[50:51], 0
	s_waitcnt lgkmcnt(0)
	s_waitcnt vmcnt(0)
	s_add_u32 s4, s48, s50
	s_addc_u32 s5, s49, s51
	s_add_u32 s75, s4, 0x100
	s_addc_u32 s76, s5, 0
	s_add_u32 s52, s72, s50
	s_addc_u32 s53, s73, s51
	s_add_u32 s4, s4, 0x180
	s_addc_u32 s5, s5, 0
	s_add_i32 s77, 0, 0x10000
	s_add_i32 s78, 0, 0x14000
	s_cmpk_eq_i32 s50, 0x1f00
	s_cselect_b32 s13, s71, s5
	s_cselect_b32 s12, s70, s4
	s_cselect_b32 s53, s37, s53
	s_cselect_b32 s52, s69, s52
	s_cselect_b32 s5, s41, s76
	s_cselect_b32 s4, s68, s75
	v_lshl_add_u64 v[214:215], v[112:113], 0, s[50:51]
	s_add_i32 m0, s17, 0xc000
	s_nop 0
	global_load_lds_dwordx4 v[214:215], off
	v_lshl_add_u64 v[214:215], v[114:115], 0, s[50:51]
	s_add_i32 m0, s17, 0xe000
	s_nop 0
	global_load_lds_dwordx4 v[214:215], off
	v_add_u32_e32 v148, s77, v203
	v_add_u32_e32 v164, s78, v203
	ds_read_b128 v[120:123], v148
	ds_read_b128 v[132:135], v148 offset:1024
	ds_read_b128 v[144:147], v148 offset:2048
	ds_read_b128 v[148:151], v148 offset:3072
	ds_read_b128 v[152:155], v164
	ds_read_b128 v[156:159], v164 offset:1024
	ds_read_b128 v[160:163], v164 offset:2048
	ds_read_b128 v[164:167], v164 offset:3072
	ds_read_b128 v[168:171], v233
	ds_read_b128 v[172:175], v233 offset:1024
	ds_read_b128 v[176:179], v233 offset:2048
	ds_read_b128 v[180:183], v233 offset:3072
	ds_read_b128 v[184:187], v233 offset:4096
	ds_read_b128 v[188:191], v233 offset:5120
	ds_read_b128 v[192:195], v233 offset:6144
	ds_read_b128 v[196:199], v233 offset:7168
	s_waitcnt vmcnt(8)
	s_waitcnt lgkmcnt(0)
	s_barrier
	s_setprio 1
	v_mfma_f32_16x16x32_bf16 v[140:143], v[120:123], v[168:171], 0
	v_mfma_f32_16x16x32_bf16 v[136:139], v[144:147], v[168:171], 0
	v_mfma_f32_16x16x32_bf16 v[116:119], v[120:123], v[176:179], 0
	v_mfma_f32_16x16x32_bf16 v[108:111], v[144:147], v[176:179], 0
	v_mfma_f32_16x16x32_bf16 v[96:99], v[120:123], v[184:187], 0
	v_mfma_f32_16x16x32_bf16 v[92:95], v[144:147], v[184:187], 0
	v_mfma_f32_16x16x32_bf16 v[80:83], v[120:123], v[192:195], 0
	v_mfma_f32_16x16x32_bf16 v[76:79], v[144:147], v[192:195], 0
	v_mfma_f32_16x16x32_bf16 v[140:143], v[132:135], v[172:175], v[140:143]
	v_mfma_f32_16x16x32_bf16 v[136:139], v[148:151], v[172:175], v[136:139]
	v_mfma_f32_16x16x32_bf16 v[116:119], v[132:135], v[180:183], v[116:119]
	v_mfma_f32_16x16x32_bf16 v[108:111], v[148:151], v[180:183], v[108:111]
	v_mfma_f32_16x16x32_bf16 v[96:99], v[132:135], v[188:191], v[96:99]
	v_mfma_f32_16x16x32_bf16 v[92:95], v[148:151], v[188:191], v[92:95]
	v_mfma_f32_16x16x32_bf16 v[80:83], v[132:135], v[196:199], v[80:83]
	v_mfma_f32_16x16x32_bf16 v[76:79], v[148:151], v[196:199], v[76:79]
	v_mfma_f32_16x16x32_bf16 v[128:131], v[152:155], v[168:171], 0
	v_mfma_f32_16x16x32_bf16 v[124:127], v[160:163], v[168:171], 0
	v_mfma_f32_16x16x32_bf16 v[104:107], v[152:155], v[176:179], 0
	v_mfma_f32_16x16x32_bf16 v[100:103], v[160:163], v[176:179], 0
	v_mfma_f32_16x16x32_bf16 v[88:91], v[152:155], v[184:187], 0
	v_mfma_f32_16x16x32_bf16 v[84:87], v[160:163], v[184:187], 0
	v_mfma_f32_16x16x32_bf16 v[72:75], v[152:155], v[192:195], 0
	v_mfma_f32_16x16x32_bf16 v[68:71], v[160:163], v[192:195], 0
	v_mfma_f32_16x16x32_bf16 v[128:131], v[156:159], v[172:175], v[128:131]
	v_mfma_f32_16x16x32_bf16 v[124:127], v[164:167], v[172:175], v[124:127]
	v_mfma_f32_16x16x32_bf16 v[104:107], v[156:159], v[180:183], v[104:107]
	v_mfma_f32_16x16x32_bf16 v[100:103], v[164:167], v[180:183], v[100:103]
	v_mfma_f32_16x16x32_bf16 v[88:91], v[156:159], v[188:191], v[88:91]
	v_mfma_f32_16x16x32_bf16 v[84:87], v[164:167], v[188:191], v[84:87]
	v_mfma_f32_16x16x32_bf16 v[72:75], v[156:159], v[196:199], v[72:75]
	v_mfma_f32_16x16x32_bf16 v[68:71], v[164:167], v[196:199], v[68:71]
	s_setprio 0
	s_barrier
	s_add_i32 s75, s77, s16
	v_lshl_add_u64 v[214:215], s[52:53], 0, v[2:3]
	s_mov_b32 m0, s75
	s_nop 0
	global_load_lds_dwordx4 v[214:215], off
	s_add_i32 m0, s75, 0x2000
	s_add_u32 s76, s52, 0x100000
	v_lshl_add_u64 v[216:217], s[52:53], 0, v[204:205]
	s_addc_u32 s77, s53, 0
	s_add_i32 s75, s78, s16
	global_load_lds_dwordx4 v[216:217], off
	v_lshl_add_u64 v[218:219], s[76:77], 0, v[2:3]
	s_mov_b32 m0, s75
	s_nop 0
	global_load_lds_dwordx4 v[218:219], off
	v_lshl_add_u64 v[218:219], s[76:77], 0, v[204:205]
	s_add_i32 m0, s75, 0x2000
	s_nop 0
	global_load_lds_dwordx4 v[218:219], off
	v_lshl_add_u64 v[218:219], s[4:5], 0, v[208:209]
	s_mov_b32 m0, s17
	s_nop 0
	global_load_lds_dwordx4 v[218:219], off
	v_lshl_add_u64 v[218:219], s[4:5], 0, v[206:207]
	s_mov_b32 m0, s46
	s_nop 0
	global_load_lds_dwordx4 v[218:219], off
	ds_read_b128 v[168:171], v233 offset:16384
	ds_read_b128 v[172:175], v233 offset:17408
	ds_read_b128 v[176:179], v233 offset:18432
	ds_read_b128 v[180:183], v233 offset:19456
	ds_read_b128 v[184:187], v233 offset:20480
	ds_read_b128 v[188:191], v233 offset:21504
	ds_read_b128 v[192:195], v233 offset:22528
	ds_read_b128 v[196:199], v233 offset:23552
	s_waitcnt vmcnt(8)
	s_waitcnt lgkmcnt(0)
	s_barrier
	s_setprio 1
	v_mfma_f32_16x16x32_bf16 v[64:67], v[120:123], v[168:171], 0
	v_mfma_f32_16x16x32_bf16 v[60:63], v[144:147], v[168:171], 0
	v_mfma_f32_16x16x32_bf16 v[48:51], v[120:123], v[176:179], 0
	v_mfma_f32_16x16x32_bf16 v[44:47], v[144:147], v[176:179], 0
	v_mfma_f32_16x16x32_bf16 v[32:35], v[120:123], v[184:187], 0
	v_mfma_f32_16x16x32_bf16 v[28:31], v[144:147], v[184:187], 0
	v_mfma_f32_16x16x32_bf16 v[16:19], v[120:123], v[192:195], 0
	v_mfma_f32_16x16x32_bf16 v[12:15], v[144:147], v[192:195], 0
	v_mfma_f32_16x16x32_bf16 v[64:67], v[132:135], v[172:175], v[64:67]
	v_mfma_f32_16x16x32_bf16 v[60:63], v[148:151], v[172:175], v[60:63]
	v_mfma_f32_16x16x32_bf16 v[48:51], v[132:135], v[180:183], v[48:51]
	v_mfma_f32_16x16x32_bf16 v[44:47], v[148:151], v[180:183], v[44:47]
	v_mfma_f32_16x16x32_bf16 v[32:35], v[132:135], v[188:191], v[32:35]
	v_mfma_f32_16x16x32_bf16 v[28:31], v[148:151], v[188:191], v[28:31]
	v_mfma_f32_16x16x32_bf16 v[16:19], v[132:135], v[196:199], v[16:19]
	v_mfma_f32_16x16x32_bf16 v[12:15], v[148:151], v[196:199], v[12:15]
	v_mfma_f32_16x16x32_bf16 v[56:59], v[152:155], v[168:171], 0
	v_mfma_f32_16x16x32_bf16 v[52:55], v[160:163], v[168:171], 0
	v_mfma_f32_16x16x32_bf16 v[40:43], v[152:155], v[176:179], 0
	v_mfma_f32_16x16x32_bf16 v[36:39], v[160:163], v[176:179], 0
	v_mfma_f32_16x16x32_bf16 v[24:27], v[152:155], v[184:187], 0
	v_mfma_f32_16x16x32_bf16 v[20:23], v[160:163], v[184:187], 0
	v_mfma_f32_16x16x32_bf16 v[8:11], v[152:155], v[192:195], 0
	v_mfma_f32_16x16x32_bf16 v[4:7], v[160:163], v[192:195], 0
	v_mfma_f32_16x16x32_bf16 v[56:59], v[156:159], v[172:175], v[56:59]
	v_mfma_f32_16x16x32_bf16 v[52:55], v[164:167], v[172:175], v[52:55]
	v_mfma_f32_16x16x32_bf16 v[40:43], v[156:159], v[180:183], v[40:43]
	v_mfma_f32_16x16x32_bf16 v[36:39], v[164:167], v[180:183], v[36:39]
	v_mfma_f32_16x16x32_bf16 v[24:27], v[156:159], v[188:191], v[24:27]
	v_mfma_f32_16x16x32_bf16 v[20:23], v[164:167], v[188:191], v[20:23]
	v_mfma_f32_16x16x32_bf16 v[8:11], v[156:159], v[196:199], v[8:11]
	v_mfma_f32_16x16x32_bf16 v[4:7], v[164:167], v[196:199], v[4:7]
	s_setprio 0
	s_barrier
	s_add_i32 s75, 0, 0x18000
	s_add_i32 s76, 0, 0x1c000
	s_add_u32 s4, s4, 0x100000
	s_addc_u32 s5, s5, 0
	s_mov_b32 m0, s47
	v_lshl_add_u64 v[218:219], s[4:5], 0, v[208:209]
	global_load_lds_dwordx4 v[218:219], off
	v_lshl_add_u64 v[218:219], s[4:5], 0, v[206:207]
	s_mov_b32 m0, s58
	s_nop 0
	global_load_lds_dwordx4 v[218:219], off
	v_add_u32_e32 v148, s75, v203
	v_add_u32_e32 v164, s76, v203
	ds_read_b128 v[120:123], v148
	ds_read_b128 v[132:135], v148 offset:1024
	ds_read_b128 v[144:147], v148 offset:2048
	ds_read_b128 v[148:151], v148 offset:3072
	ds_read_b128 v[152:155], v164
	ds_read_b128 v[156:159], v164 offset:1024
	ds_read_b128 v[160:163], v164 offset:2048
	ds_read_b128 v[164:167], v164 offset:3072
	ds_read_b128 v[168:171], v233 offset:32768
	ds_read_b128 v[172:175], v233 offset:33792
	ds_read_b128 v[176:179], v233 offset:34816
	ds_read_b128 v[180:183], v233 offset:35840
	ds_read_b128 v[184:187], v233 offset:36864
	ds_read_b128 v[188:191], v233 offset:37888
	ds_read_b128 v[192:195], v233 offset:38912
	ds_read_b128 v[196:199], v233 offset:39936
	s_waitcnt vmcnt(8)
	s_waitcnt lgkmcnt(0)
	s_barrier
	s_setprio 1
	v_mfma_f32_16x16x32_bf16 v[140:143], v[120:123], v[168:171], v[140:143]
	v_mfma_f32_16x16x32_bf16 v[136:139], v[144:147], v[168:171], v[136:139]
	v_mfma_f32_16x16x32_bf16 v[116:119], v[120:123], v[176:179], v[116:119]
	v_mfma_f32_16x16x32_bf16 v[108:111], v[144:147], v[176:179], v[108:111]
	v_mfma_f32_16x16x32_bf16 v[96:99], v[120:123], v[184:187], v[96:99]
	v_mfma_f32_16x16x32_bf16 v[92:95], v[144:147], v[184:187], v[92:95]
	v_mfma_f32_16x16x32_bf16 v[80:83], v[120:123], v[192:195], v[80:83]
	v_mfma_f32_16x16x32_bf16 v[76:79], v[144:147], v[192:195], v[76:79]
	v_mfma_f32_16x16x32_bf16 v[140:143], v[132:135], v[172:175], v[140:143]
	v_mfma_f32_16x16x32_bf16 v[136:139], v[148:151], v[172:175], v[136:139]
	v_mfma_f32_16x16x32_bf16 v[116:119], v[132:135], v[180:183], v[116:119]
	v_mfma_f32_16x16x32_bf16 v[108:111], v[148:151], v[180:183], v[108:111]
	v_mfma_f32_16x16x32_bf16 v[96:99], v[132:135], v[188:191], v[96:99]
	v_mfma_f32_16x16x32_bf16 v[92:95], v[148:151], v[188:191], v[92:95]
	v_mfma_f32_16x16x32_bf16 v[80:83], v[132:135], v[196:199], v[80:83]
	v_mfma_f32_16x16x32_bf16 v[76:79], v[148:151], v[196:199], v[76:79]
	v_mfma_f32_16x16x32_bf16 v[128:131], v[152:155], v[168:171], v[128:131]
	v_mfma_f32_16x16x32_bf16 v[124:127], v[160:163], v[168:171], v[124:127]
	v_mfma_f32_16x16x32_bf16 v[104:107], v[152:155], v[176:179], v[104:107]
	v_mfma_f32_16x16x32_bf16 v[100:103], v[160:163], v[176:179], v[100:103]
	v_mfma_f32_16x16x32_bf16 v[88:91], v[152:155], v[184:187], v[88:91]
	v_mfma_f32_16x16x32_bf16 v[84:87], v[160:163], v[184:187], v[84:87]
	v_mfma_f32_16x16x32_bf16 v[72:75], v[152:155], v[192:195], v[72:75]
	v_mfma_f32_16x16x32_bf16 v[68:71], v[160:163], v[192:195], v[68:71]
	v_mfma_f32_16x16x32_bf16 v[128:131], v[156:159], v[172:175], v[128:131]
	v_mfma_f32_16x16x32_bf16 v[124:127], v[164:167], v[172:175], v[124:127]
	v_mfma_f32_16x16x32_bf16 v[104:107], v[156:159], v[180:183], v[104:107]
	v_mfma_f32_16x16x32_bf16 v[100:103], v[164:167], v[180:183], v[100:103]
	v_mfma_f32_16x16x32_bf16 v[88:91], v[156:159], v[188:191], v[88:91]
	v_mfma_f32_16x16x32_bf16 v[84:87], v[164:167], v[188:191], v[84:87]
	v_mfma_f32_16x16x32_bf16 v[72:75], v[156:159], v[196:199], v[72:75]
	v_mfma_f32_16x16x32_bf16 v[68:71], v[164:167], v[196:199], v[68:71]
	s_setprio 0
	s_barrier
	s_add_i32 s4, s75, s16
	v_lshl_add_u64 v[214:215], v[214:215], 0, s[34:35]
	s_mov_b32 m0, s4
	s_nop 0
	global_load_lds_dwordx4 v[214:215], off
	s_add_i32 m0, s4, 0x2000
	s_add_u32 s4, s52, 0x100080
	v_lshl_add_u64 v[214:215], v[216:217], 0, s[34:35]
	s_addc_u32 s5, s53, 0
	s_add_i32 s52, s76, s16
	global_load_lds_dwordx4 v[214:215], off
	v_lshl_add_u64 v[214:215], s[4:5], 0, v[2:3]
	s_mov_b32 m0, s52
	s_nop 0
	global_load_lds_dwordx4 v[214:215], off
	v_lshl_add_u64 v[214:215], s[4:5], 0, v[204:205]
	s_add_i32 m0, s52, 0x2000
	s_nop 0
	global_load_lds_dwordx4 v[214:215], off
	v_lshl_add_u64 v[214:215], s[12:13], 0, v[208:209]
	s_mov_b32 m0, s62
	s_nop 0
	global_load_lds_dwordx4 v[214:215], off
	v_lshl_add_u64 v[214:215], s[12:13], 0, v[206:207]
	s_mov_b32 m0, s63
	s_nop 0
	global_load_lds_dwordx4 v[214:215], off
	ds_read_b128 v[168:171], v233 offset:49152
	ds_read_b128 v[172:175], v233 offset:50176
	ds_read_b128 v[176:179], v233 offset:51200
	ds_read_b128 v[180:183], v233 offset:52224
	ds_read_b128 v[184:187], v233 offset:53248
	ds_read_b128 v[188:191], v233 offset:54272
	ds_read_b128 v[192:195], v233 offset:55296
	ds_read_b128 v[196:199], v233 offset:56320
	s_waitcnt vmcnt(8)
	s_waitcnt lgkmcnt(0)
	s_barrier
	s_setprio 1
	v_mfma_f32_16x16x32_bf16 v[64:67], v[120:123], v[168:171], v[64:67]
	v_mfma_f32_16x16x32_bf16 v[60:63], v[144:147], v[168:171], v[60:63]
	v_mfma_f32_16x16x32_bf16 v[48:51], v[120:123], v[176:179], v[48:51]
	v_mfma_f32_16x16x32_bf16 v[44:47], v[144:147], v[176:179], v[44:47]
	v_mfma_f32_16x16x32_bf16 v[32:35], v[120:123], v[184:187], v[32:35]
	v_mfma_f32_16x16x32_bf16 v[28:31], v[144:147], v[184:187], v[28:31]
	v_mfma_f32_16x16x32_bf16 v[16:19], v[120:123], v[192:195], v[16:19]
	v_mfma_f32_16x16x32_bf16 v[12:15], v[144:147], v[192:195], v[12:15]
	v_mfma_f32_16x16x32_bf16 v[64:67], v[132:135], v[172:175], v[64:67]
	v_mfma_f32_16x16x32_bf16 v[60:63], v[148:151], v[172:175], v[60:63]
	v_mfma_f32_16x16x32_bf16 v[48:51], v[132:135], v[180:183], v[48:51]
	v_mfma_f32_16x16x32_bf16 v[44:47], v[148:151], v[180:183], v[44:47]
	v_mfma_f32_16x16x32_bf16 v[32:35], v[132:135], v[188:191], v[32:35]
	v_mfma_f32_16x16x32_bf16 v[28:31], v[148:151], v[188:191], v[28:31]
	v_mfma_f32_16x16x32_bf16 v[16:19], v[132:135], v[196:199], v[16:19]
	v_mfma_f32_16x16x32_bf16 v[12:15], v[148:151], v[196:199], v[12:15]
	v_mfma_f32_16x16x32_bf16 v[56:59], v[152:155], v[168:171], v[56:59]
	v_mfma_f32_16x16x32_bf16 v[52:55], v[160:163], v[168:171], v[52:55]
	v_mfma_f32_16x16x32_bf16 v[40:43], v[152:155], v[176:179], v[40:43]
	v_mfma_f32_16x16x32_bf16 v[36:39], v[160:163], v[176:179], v[36:39]
	v_mfma_f32_16x16x32_bf16 v[24:27], v[152:155], v[184:187], v[24:27]
	v_mfma_f32_16x16x32_bf16 v[20:23], v[160:163], v[184:187], v[20:23]
	v_mfma_f32_16x16x32_bf16 v[8:11], v[152:155], v[192:195], v[8:11]
	v_mfma_f32_16x16x32_bf16 v[4:7], v[160:163], v[192:195], v[4:7]
	v_mfma_f32_16x16x32_bf16 v[56:59], v[156:159], v[172:175], v[56:59]
	v_mfma_f32_16x16x32_bf16 v[52:55], v[164:167], v[172:175], v[52:55]
	v_mfma_f32_16x16x32_bf16 v[40:43], v[156:159], v[180:183], v[40:43]
	v_mfma_f32_16x16x32_bf16 v[36:39], v[164:167], v[180:183], v[36:39]
	v_mfma_f32_16x16x32_bf16 v[24:27], v[156:159], v[188:191], v[24:27]
	v_mfma_f32_16x16x32_bf16 v[20:23], v[164:167], v[188:191], v[20:23]
	v_mfma_f32_16x16x32_bf16 v[8:11], v[156:159], v[196:199], v[8:11]
	v_mfma_f32_16x16x32_bf16 v[4:7], v[164:167], v[196:199], v[4:7]
	s_setprio 0
	s_barrier
	s_add_i32 s74, s74, 2
	s_add_u32 s50, s50, 0x100
	s_addc_u32 s51, s51, 0
	s_cmp_gt_u32 s74, 61
.LBB0_1459:
	s_add_u32 s4, s48, s50
	s_addc_u32 s5, s49, s51
	s_add_u32 s75, s4, 0x100
	s_addc_u32 s76, s5, 0
	s_add_u32 s52, s72, s50
	s_addc_u32 s53, s73, s51
	s_add_u32 s4, s4, 0x180
	s_addc_u32 s5, s5, 0
	s_add_i32 s77, 0, 0x10000
	s_add_i32 s78, 0, 0x14000
	s_cmpk_eq_i32 s50, 0x1f00
	s_cselect_b32 s13, s71, s5
	s_cselect_b32 s12, s70, s4
	s_cselect_b32 s53, s37, s53
	s_cselect_b32 s52, s69, s52
	s_cselect_b32 s5, s41, s76
	s_cselect_b32 s4, s68, s75
	v_lshl_add_u64 v[214:215], v[112:113], 0, s[50:51]
	s_add_i32 m0, s17, 0xc000
	s_nop 0
	global_load_lds_dwordx4 v[214:215], off
	v_lshl_add_u64 v[214:215], v[114:115], 0, s[50:51]
	s_add_i32 m0, s17, 0xe000
	s_nop 0
	global_load_lds_dwordx4 v[214:215], off
	v_add_u32_e32 v148, s77, v203
	v_add_u32_e32 v164, s78, v203
	ds_read_b128 v[120:123], v148
	ds_read_b128 v[132:135], v148 offset:1024
	ds_read_b128 v[144:147], v148 offset:2048
	ds_read_b128 v[148:151], v148 offset:3072
	ds_read_b128 v[152:155], v164
	ds_read_b128 v[156:159], v164 offset:1024
	ds_read_b128 v[160:163], v164 offset:2048
	ds_read_b128 v[164:167], v164 offset:3072
	ds_read_b128 v[168:171], v233
	ds_read_b128 v[172:175], v233 offset:1024
	ds_read_b128 v[176:179], v233 offset:2048
	ds_read_b128 v[180:183], v233 offset:3072
	ds_read_b128 v[184:187], v233 offset:4096
	ds_read_b128 v[188:191], v233 offset:5120
	ds_read_b128 v[192:195], v233 offset:6144
	ds_read_b128 v[196:199], v233 offset:7168
	s_waitcnt vmcnt(8)
	s_waitcnt lgkmcnt(0)
	s_barrier
	s_setprio 1
	v_mfma_f32_16x16x32_bf16 v[140:143], v[120:123], v[168:171], v[140:143]
	v_mfma_f32_16x16x32_bf16 v[136:139], v[144:147], v[168:171], v[136:139]
	v_mfma_f32_16x16x32_bf16 v[116:119], v[120:123], v[176:179], v[116:119]
	v_mfma_f32_16x16x32_bf16 v[108:111], v[144:147], v[176:179], v[108:111]
	v_mfma_f32_16x16x32_bf16 v[96:99], v[120:123], v[184:187], v[96:99]
	v_mfma_f32_16x16x32_bf16 v[92:95], v[144:147], v[184:187], v[92:95]
	v_mfma_f32_16x16x32_bf16 v[80:83], v[120:123], v[192:195], v[80:83]
	v_mfma_f32_16x16x32_bf16 v[76:79], v[144:147], v[192:195], v[76:79]
	v_mfma_f32_16x16x32_bf16 v[140:143], v[132:135], v[172:175], v[140:143]
	v_mfma_f32_16x16x32_bf16 v[136:139], v[148:151], v[172:175], v[136:139]
	v_mfma_f32_16x16x32_bf16 v[116:119], v[132:135], v[180:183], v[116:119]
	v_mfma_f32_16x16x32_bf16 v[108:111], v[148:151], v[180:183], v[108:111]
	v_mfma_f32_16x16x32_bf16 v[96:99], v[132:135], v[188:191], v[96:99]
	v_mfma_f32_16x16x32_bf16 v[92:95], v[148:151], v[188:191], v[92:95]
	v_mfma_f32_16x16x32_bf16 v[80:83], v[132:135], v[196:199], v[80:83]
	v_mfma_f32_16x16x32_bf16 v[76:79], v[148:151], v[196:199], v[76:79]
	v_mfma_f32_16x16x32_bf16 v[128:131], v[152:155], v[168:171], v[128:131]
	v_mfma_f32_16x16x32_bf16 v[124:127], v[160:163], v[168:171], v[124:127]
	v_mfma_f32_16x16x32_bf16 v[104:107], v[152:155], v[176:179], v[104:107]
	v_mfma_f32_16x16x32_bf16 v[100:103], v[160:163], v[176:179], v[100:103]
	v_mfma_f32_16x16x32_bf16 v[88:91], v[152:155], v[184:187], v[88:91]
	v_mfma_f32_16x16x32_bf16 v[84:87], v[160:163], v[184:187], v[84:87]
	v_mfma_f32_16x16x32_bf16 v[72:75], v[152:155], v[192:195], v[72:75]
	v_mfma_f32_16x16x32_bf16 v[68:71], v[160:163], v[192:195], v[68:71]
	v_mfma_f32_16x16x32_bf16 v[128:131], v[156:159], v[172:175], v[128:131]
	v_mfma_f32_16x16x32_bf16 v[124:127], v[164:167], v[172:175], v[124:127]
	v_mfma_f32_16x16x32_bf16 v[104:107], v[156:159], v[180:183], v[104:107]
	v_mfma_f32_16x16x32_bf16 v[100:103], v[164:167], v[180:183], v[100:103]
	v_mfma_f32_16x16x32_bf16 v[88:91], v[156:159], v[188:191], v[88:91]
	v_mfma_f32_16x16x32_bf16 v[84:87], v[164:167], v[188:191], v[84:87]
	v_mfma_f32_16x16x32_bf16 v[72:75], v[156:159], v[196:199], v[72:75]
	v_mfma_f32_16x16x32_bf16 v[68:71], v[164:167], v[196:199], v[68:71]
	s_setprio 0
	s_barrier
	s_add_i32 s75, s77, s16
	v_lshl_add_u64 v[214:215], s[52:53], 0, v[2:3]
	s_mov_b32 m0, s75
	s_nop 0
	global_load_lds_dwordx4 v[214:215], off
	s_add_i32 m0, s75, 0x2000
	s_add_u32 s76, s52, 0x100000
	v_lshl_add_u64 v[216:217], s[52:53], 0, v[204:205]
	s_addc_u32 s77, s53, 0
	s_add_i32 s75, s78, s16
	global_load_lds_dwordx4 v[216:217], off
	v_lshl_add_u64 v[218:219], s[76:77], 0, v[2:3]
	s_mov_b32 m0, s75
	s_nop 0
	global_load_lds_dwordx4 v[218:219], off
	v_lshl_add_u64 v[218:219], s[76:77], 0, v[204:205]
	s_add_i32 m0, s75, 0x2000
	s_nop 0
	global_load_lds_dwordx4 v[218:219], off
	v_lshl_add_u64 v[218:219], s[4:5], 0, v[208:209]
	s_mov_b32 m0, s17
	s_nop 0
	global_load_lds_dwordx4 v[218:219], off
	v_lshl_add_u64 v[218:219], s[4:5], 0, v[206:207]
	s_mov_b32 m0, s46
	s_nop 0
	global_load_lds_dwordx4 v[218:219], off
	ds_read_b128 v[168:171], v233 offset:16384
	ds_read_b128 v[172:175], v233 offset:17408
	ds_read_b128 v[176:179], v233 offset:18432
	ds_read_b128 v[180:183], v233 offset:19456
	ds_read_b128 v[184:187], v233 offset:20480
	ds_read_b128 v[188:191], v233 offset:21504
	ds_read_b128 v[192:195], v233 offset:22528
	ds_read_b128 v[196:199], v233 offset:23552
	s_waitcnt vmcnt(8)
	s_waitcnt lgkmcnt(0)
	s_barrier
	s_setprio 1
	v_mfma_f32_16x16x32_bf16 v[64:67], v[120:123], v[168:171], v[64:67]
	v_mfma_f32_16x16x32_bf16 v[60:63], v[144:147], v[168:171], v[60:63]
	v_mfma_f32_16x16x32_bf16 v[48:51], v[120:123], v[176:179], v[48:51]
	v_mfma_f32_16x16x32_bf16 v[44:47], v[144:147], v[176:179], v[44:47]
	v_mfma_f32_16x16x32_bf16 v[32:35], v[120:123], v[184:187], v[32:35]
	v_mfma_f32_16x16x32_bf16 v[28:31], v[144:147], v[184:187], v[28:31]
	v_mfma_f32_16x16x32_bf16 v[16:19], v[120:123], v[192:195], v[16:19]
	v_mfma_f32_16x16x32_bf16 v[12:15], v[144:147], v[192:195], v[12:15]
	v_mfma_f32_16x16x32_bf16 v[64:67], v[132:135], v[172:175], v[64:67]
	v_mfma_f32_16x16x32_bf16 v[60:63], v[148:151], v[172:175], v[60:63]
	v_mfma_f32_16x16x32_bf16 v[48:51], v[132:135], v[180:183], v[48:51]
	v_mfma_f32_16x16x32_bf16 v[44:47], v[148:151], v[180:183], v[44:47]
	v_mfma_f32_16x16x32_bf16 v[32:35], v[132:135], v[188:191], v[32:35]
	v_mfma_f32_16x16x32_bf16 v[28:31], v[148:151], v[188:191], v[28:31]
	v_mfma_f32_16x16x32_bf16 v[16:19], v[132:135], v[196:199], v[16:19]
	v_mfma_f32_16x16x32_bf16 v[12:15], v[148:151], v[196:199], v[12:15]
	v_mfma_f32_16x16x32_bf16 v[56:59], v[152:155], v[168:171], v[56:59]
	v_mfma_f32_16x16x32_bf16 v[52:55], v[160:163], v[168:171], v[52:55]
	v_mfma_f32_16x16x32_bf16 v[40:43], v[152:155], v[176:179], v[40:43]
	v_mfma_f32_16x16x32_bf16 v[36:39], v[160:163], v[176:179], v[36:39]
	v_mfma_f32_16x16x32_bf16 v[24:27], v[152:155], v[184:187], v[24:27]
	v_mfma_f32_16x16x32_bf16 v[20:23], v[160:163], v[184:187], v[20:23]
	v_mfma_f32_16x16x32_bf16 v[8:11], v[152:155], v[192:195], v[8:11]
	v_mfma_f32_16x16x32_bf16 v[4:7], v[160:163], v[192:195], v[4:7]
	v_mfma_f32_16x16x32_bf16 v[56:59], v[156:159], v[172:175], v[56:59]
	v_mfma_f32_16x16x32_bf16 v[52:55], v[164:167], v[172:175], v[52:55]
	v_mfma_f32_16x16x32_bf16 v[40:43], v[156:159], v[180:183], v[40:43]
	v_mfma_f32_16x16x32_bf16 v[36:39], v[164:167], v[180:183], v[36:39]
	v_mfma_f32_16x16x32_bf16 v[24:27], v[156:159], v[188:191], v[24:27]
	v_mfma_f32_16x16x32_bf16 v[20:23], v[164:167], v[188:191], v[20:23]
	v_mfma_f32_16x16x32_bf16 v[8:11], v[156:159], v[196:199], v[8:11]
	v_mfma_f32_16x16x32_bf16 v[4:7], v[164:167], v[196:199], v[4:7]
	s_setprio 0
	s_barrier
	s_add_i32 s75, 0, 0x18000
	s_add_i32 s76, 0, 0x1c000
	s_add_u32 s4, s4, 0x100000
	s_addc_u32 s5, s5, 0
	s_mov_b32 m0, s47
	v_lshl_add_u64 v[218:219], s[4:5], 0, v[208:209]
	global_load_lds_dwordx4 v[218:219], off
	v_lshl_add_u64 v[218:219], s[4:5], 0, v[206:207]
	s_mov_b32 m0, s58
	s_nop 0
	global_load_lds_dwordx4 v[218:219], off
	v_add_u32_e32 v148, s75, v203
	v_add_u32_e32 v164, s76, v203
	ds_read_b128 v[120:123], v148
	ds_read_b128 v[132:135], v148 offset:1024
	ds_read_b128 v[144:147], v148 offset:2048
	ds_read_b128 v[148:151], v148 offset:3072
	ds_read_b128 v[152:155], v164
	ds_read_b128 v[156:159], v164 offset:1024
	ds_read_b128 v[160:163], v164 offset:2048
	ds_read_b128 v[164:167], v164 offset:3072
	ds_read_b128 v[168:171], v233 offset:32768
	ds_read_b128 v[172:175], v233 offset:33792
	ds_read_b128 v[176:179], v233 offset:34816
	ds_read_b128 v[180:183], v233 offset:35840
	ds_read_b128 v[184:187], v233 offset:36864
	ds_read_b128 v[188:191], v233 offset:37888
	ds_read_b128 v[192:195], v233 offset:38912
	ds_read_b128 v[196:199], v233 offset:39936
	s_waitcnt vmcnt(8)
	s_waitcnt lgkmcnt(0)
	s_barrier
	s_setprio 1
	v_mfma_f32_16x16x32_bf16 v[140:143], v[120:123], v[168:171], v[140:143]
	v_mfma_f32_16x16x32_bf16 v[136:139], v[144:147], v[168:171], v[136:139]
	v_mfma_f32_16x16x32_bf16 v[116:119], v[120:123], v[176:179], v[116:119]
	v_mfma_f32_16x16x32_bf16 v[108:111], v[144:147], v[176:179], v[108:111]
	v_mfma_f32_16x16x32_bf16 v[96:99], v[120:123], v[184:187], v[96:99]
	v_mfma_f32_16x16x32_bf16 v[92:95], v[144:147], v[184:187], v[92:95]
	v_mfma_f32_16x16x32_bf16 v[80:83], v[120:123], v[192:195], v[80:83]
	v_mfma_f32_16x16x32_bf16 v[76:79], v[144:147], v[192:195], v[76:79]
	v_mfma_f32_16x16x32_bf16 v[140:143], v[132:135], v[172:175], v[140:143]
	v_mfma_f32_16x16x32_bf16 v[136:139], v[148:151], v[172:175], v[136:139]
	v_mfma_f32_16x16x32_bf16 v[116:119], v[132:135], v[180:183], v[116:119]
	v_mfma_f32_16x16x32_bf16 v[108:111], v[148:151], v[180:183], v[108:111]
	v_mfma_f32_16x16x32_bf16 v[96:99], v[132:135], v[188:191], v[96:99]
	v_mfma_f32_16x16x32_bf16 v[92:95], v[148:151], v[188:191], v[92:95]
	v_mfma_f32_16x16x32_bf16 v[80:83], v[132:135], v[196:199], v[80:83]
	v_mfma_f32_16x16x32_bf16 v[76:79], v[148:151], v[196:199], v[76:79]
	v_mfma_f32_16x16x32_bf16 v[128:131], v[152:155], v[168:171], v[128:131]
	v_mfma_f32_16x16x32_bf16 v[124:127], v[160:163], v[168:171], v[124:127]
	v_mfma_f32_16x16x32_bf16 v[104:107], v[152:155], v[176:179], v[104:107]
	v_mfma_f32_16x16x32_bf16 v[100:103], v[160:163], v[176:179], v[100:103]
	v_mfma_f32_16x16x32_bf16 v[88:91], v[152:155], v[184:187], v[88:91]
	v_mfma_f32_16x16x32_bf16 v[84:87], v[160:163], v[184:187], v[84:87]
	v_mfma_f32_16x16x32_bf16 v[72:75], v[152:155], v[192:195], v[72:75]
	v_mfma_f32_16x16x32_bf16 v[68:71], v[160:163], v[192:195], v[68:71]
	v_mfma_f32_16x16x32_bf16 v[128:131], v[156:159], v[172:175], v[128:131]
	v_mfma_f32_16x16x32_bf16 v[124:127], v[164:167], v[172:175], v[124:127]
	v_mfma_f32_16x16x32_bf16 v[104:107], v[156:159], v[180:183], v[104:107]
	v_mfma_f32_16x16x32_bf16 v[100:103], v[164:167], v[180:183], v[100:103]
	v_mfma_f32_16x16x32_bf16 v[88:91], v[156:159], v[188:191], v[88:91]
	v_mfma_f32_16x16x32_bf16 v[84:87], v[164:167], v[188:191], v[84:87]
	v_mfma_f32_16x16x32_bf16 v[72:75], v[156:159], v[196:199], v[72:75]
	v_mfma_f32_16x16x32_bf16 v[68:71], v[164:167], v[196:199], v[68:71]
	s_setprio 0
	s_barrier
	s_add_i32 s4, s75, s16
	v_lshl_add_u64 v[214:215], v[214:215], 0, s[34:35]
	s_mov_b32 m0, s4
	s_nop 0
	global_load_lds_dwordx4 v[214:215], off
	s_add_i32 m0, s4, 0x2000
	s_add_u32 s4, s52, 0x100080
	v_lshl_add_u64 v[214:215], v[216:217], 0, s[34:35]
	s_addc_u32 s5, s53, 0
	s_add_i32 s52, s76, s16
	global_load_lds_dwordx4 v[214:215], off
	v_lshl_add_u64 v[214:215], s[4:5], 0, v[2:3]
	s_mov_b32 m0, s52
	s_nop 0
	global_load_lds_dwordx4 v[214:215], off
	v_lshl_add_u64 v[214:215], s[4:5], 0, v[204:205]
	s_add_i32 m0, s52, 0x2000
	s_nop 0
	global_load_lds_dwordx4 v[214:215], off
	v_lshl_add_u64 v[214:215], s[12:13], 0, v[208:209]
	s_mov_b32 m0, s62
	s_nop 0
	global_load_lds_dwordx4 v[214:215], off
	v_lshl_add_u64 v[214:215], s[12:13], 0, v[206:207]
	s_mov_b32 m0, s63
	s_nop 0
	global_load_lds_dwordx4 v[214:215], off
	ds_read_b128 v[168:171], v233 offset:49152
	ds_read_b128 v[172:175], v233 offset:50176
	ds_read_b128 v[176:179], v233 offset:51200
	ds_read_b128 v[180:183], v233 offset:52224
	ds_read_b128 v[184:187], v233 offset:53248
	ds_read_b128 v[188:191], v233 offset:54272
	ds_read_b128 v[192:195], v233 offset:55296
	ds_read_b128 v[196:199], v233 offset:56320
	s_waitcnt vmcnt(8)
	s_waitcnt lgkmcnt(0)
	s_barrier
	s_setprio 1
	v_mfma_f32_16x16x32_bf16 v[64:67], v[120:123], v[168:171], v[64:67]
	v_mfma_f32_16x16x32_bf16 v[60:63], v[144:147], v[168:171], v[60:63]
	v_mfma_f32_16x16x32_bf16 v[48:51], v[120:123], v[176:179], v[48:51]
	v_mfma_f32_16x16x32_bf16 v[44:47], v[144:147], v[176:179], v[44:47]
	v_mfma_f32_16x16x32_bf16 v[32:35], v[120:123], v[184:187], v[32:35]
	v_mfma_f32_16x16x32_bf16 v[28:31], v[144:147], v[184:187], v[28:31]
	v_mfma_f32_16x16x32_bf16 v[16:19], v[120:123], v[192:195], v[16:19]
	v_mfma_f32_16x16x32_bf16 v[12:15], v[144:147], v[192:195], v[12:15]
	v_mfma_f32_16x16x32_bf16 v[64:67], v[132:135], v[172:175], v[64:67]
	v_mfma_f32_16x16x32_bf16 v[60:63], v[148:151], v[172:175], v[60:63]
	v_mfma_f32_16x16x32_bf16 v[48:51], v[132:135], v[180:183], v[48:51]
	v_mfma_f32_16x16x32_bf16 v[44:47], v[148:151], v[180:183], v[44:47]
	v_mfma_f32_16x16x32_bf16 v[32:35], v[132:135], v[188:191], v[32:35]
	v_mfma_f32_16x16x32_bf16 v[28:31], v[148:151], v[188:191], v[28:31]
	v_mfma_f32_16x16x32_bf16 v[16:19], v[132:135], v[196:199], v[16:19]
	v_mfma_f32_16x16x32_bf16 v[12:15], v[148:151], v[196:199], v[12:15]
	v_mfma_f32_16x16x32_bf16 v[56:59], v[152:155], v[168:171], v[56:59]
	v_mfma_f32_16x16x32_bf16 v[52:55], v[160:163], v[168:171], v[52:55]
	v_mfma_f32_16x16x32_bf16 v[40:43], v[152:155], v[176:179], v[40:43]
	v_mfma_f32_16x16x32_bf16 v[36:39], v[160:163], v[176:179], v[36:39]
	v_mfma_f32_16x16x32_bf16 v[24:27], v[152:155], v[184:187], v[24:27]
	v_mfma_f32_16x16x32_bf16 v[20:23], v[160:163], v[184:187], v[20:23]
	v_mfma_f32_16x16x32_bf16 v[8:11], v[152:155], v[192:195], v[8:11]
	v_mfma_f32_16x16x32_bf16 v[4:7], v[160:163], v[192:195], v[4:7]
	v_mfma_f32_16x16x32_bf16 v[56:59], v[156:159], v[172:175], v[56:59]
	v_mfma_f32_16x16x32_bf16 v[52:55], v[164:167], v[172:175], v[52:55]
	v_mfma_f32_16x16x32_bf16 v[40:43], v[156:159], v[180:183], v[40:43]
	v_mfma_f32_16x16x32_bf16 v[36:39], v[164:167], v[180:183], v[36:39]
	v_mfma_f32_16x16x32_bf16 v[24:27], v[156:159], v[188:191], v[24:27]
	v_mfma_f32_16x16x32_bf16 v[20:23], v[164:167], v[188:191], v[20:23]
	v_mfma_f32_16x16x32_bf16 v[8:11], v[156:159], v[196:199], v[8:11]
	v_mfma_f32_16x16x32_bf16 v[4:7], v[164:167], v[196:199], v[4:7]
	s_setprio 0
	s_barrier
	s_add_i32 s74, s74, 2
	s_add_u32 s50, s50, 0x100
	s_addc_u32 s51, s51, 0
	s_cmp_gt_u32 s74, 61
	s_cbranch_scc0 .LBB0_1459
	s_and_b64 vcc, exec, s[22:23]
	s_cbranch_vccz .LBB0_1462
	s_barrier
